# v102 + P3 softmax (constant-bias path): mask-bit compares moved into the LUT path only; 16-value row max as 7 v_max3 + 1 v_max (no self-max canonicalisations)
# speedup vs baseline: 1.0022x; 1.0022x over previous
; #define LAS __attribute__((address_space(3)))
; __device__ __forceinline__ void attn_phase_mfma(Frame& F) {
;     ...
;             if (valid) {
;                 const int key0 = kt * 32;
;                 f32x16 s;
; #pragma unroll
;                 for (int r = 0; r < 16; ++r) s[r] = 0.f;
;                 bf16x8 kf[8];
; #pragma unroll
;                 for (int ks = 0; ks < 8; ++ks) kf[ks] = *(const LAS bf16x8*)(KB + c * AT_KPITCH + (16 * ks + 8 * hh) * 2);
;                 __builtin_amdgcn_sched_barrier(0);
; #pragma unroll
;                 for (int ks = 0; ks < 8; ++ks) s = __builtin_amdgcn_mfma_f32_32x32x16_bf16(kf[ks], qf[ks], s, 0, 0, 0);
;                 v4u vfr[4][2];
; #pragma unroll
;                 for (int db = 0; db < 4; ++db)
; #pragma unroll
;                     for (int s2 = 0; s2 < 2; ++s2) { const LAS unsigned char* vp = VB + (32 * db + c) * AT_VPITCH + (16 * s2 + 4 * hh) * 2;
;                         const v2u lo = *(const LAS v2u*)vp, hi = *(const LAS v2u*)(vp + 16); vfr[db][s2] = (v4u){lo.x, lo.y, hi.x, hi.y}; }
;                 __builtin_amdgcn_sched_barrier(0);
;                 const bool far = (q0 - key0 - 31) >= 128;
;                 const unsigned mwh = mw >> (4 * hh);
;     ...
;             if (kt + 2 <= qb) { AT_WRITE_TILE((st + 1) & 1); mw = mwn; }
.LBB0_550:
	s_mul_i32 s0, s18, 0x2200
	v_add_u32_e32 v68, s0, v221
	ds_read_b128 v[64:67], v68
	ds_read_b128 v[80:83], v68 offset:32
	ds_read_b128 v[84:87], v68 offset:64
	ds_read_b128 v[88:91], v68 offset:96
	ds_read_b128 v[92:95], v68 offset:128
	ds_read_b128 v[144:147], v68 offset:160
	ds_read_b128 v[148:151], v68 offset:192
	ds_read_b128 v[152:155], v68 offset:224
	s_waitcnt lgkmcnt(7)
	v_mfma_f32_32x32x16_bf16 v[64:79], v[64:67], v[136:139], 0
	s_mul_i32 s0, s18, 0x2400
	s_waitcnt lgkmcnt(6)
	v_mfma_f32_32x32x16_bf16 v[64:79], v[80:83], v[112:115], v[64:79]
	v_add_u32_e32 v80, s0, v226
	v_add_u32_e32 v81, 0x8800, v80
	s_waitcnt lgkmcnt(5)
	v_mfma_f32_32x32x16_bf16 v[64:79], v[84:87], v[116:119], v[64:79]
	s_waitcnt lgkmcnt(4)
	v_mfma_f32_32x32x16_bf16 v[64:79], v[88:91], v[120:123], v[64:79]
	s_waitcnt lgkmcnt(3)
	v_mfma_f32_32x32x16_bf16 v[64:79], v[92:95], v[124:127], v[64:79]
	s_waitcnt lgkmcnt(2)
	v_mfma_f32_32x32x16_bf16 v[64:79], v[144:147], v[128:131], v[64:79]
	s_waitcnt lgkmcnt(1)
	v_mfma_f32_32x32x16_bf16 v[64:79], v[148:151], v[132:135], v[64:79]
	ds_read2_b64 v[148:151], v81 offset1:2
	ds_read2_b64 v[144:147], v81 offset0:4 offset1:6
	v_add_u32_e32 v81, 0x9000, v80
	s_waitcnt lgkmcnt(2)
	v_mfma_f32_32x32x16_bf16 v[64:79], v[152:155], v[140:143], v[64:79]
	ds_read2_b64 v[152:155], v81 offset0:32 offset1:34
	ds_read2_b64 v[156:159], v81 offset0:36 offset1:38
	v_add_u32_e32 v81, 0x9800, v80
	v_add_u32_e32 v80, 0xa000, v80
	ds_read2_b64 v[164:167], v81 offset0:64 offset1:66
	ds_read2_b64 v[168:171], v81 offset0:68 offset1:70
	ds_read2_b64 v[172:175], v80 offset0:96 offset1:98
	ds_read2_b64 v[160:163], v80 offset0:100 offset1:102
	v_lshrrev_b32_e32 v233, v222, v229
	v_and_b32_e32 v199, 1, v233
	v_and_b32_e32 v198, 2, v233
	v_and_b32_e32 v242, 4, v233
	v_and_b32_e32 v250, 8, v233
	v_and_b32_e32 v249, 0x100, v233
	v_and_b32_e32 v248, 0x200, v233
	v_and_b32_e32 v244, 0x400, v233
	v_and_b32_e32 v243, 0x800, v233
	v_and_b32_e32 v241, 0x10000, v233
	v_and_b32_e32 v240, 0x20000, v233
	v_and_b32_e32 v239, 0x40000, v233
	v_and_b32_e32 v238, 0x80000, v233
	v_and_b32_e32 v237, 0x1000000, v233
	v_and_b32_e32 v236, 0x2000000, v233
	v_and_b32_e32 v235, 0x4000000, v233
	s_cmp_lt_i32 s16, s11
	s_mov_b64 s[4:5], -1
	s_cbranch_scc0 .LBB0_561
	s_branch .LBB0_562

; __device__ __forceinline__ void attn_phase_mfma(Frame& F) {
;     ...
;                 } else {
;                     float vmax = -INFINITY;
; #pragma unroll
;                     for (int r = 0; r < 16; ++r) { const int koff = (r & 3) + 8 * (r >> 2) + 4 * hh; int dist = tq - (key0 + koff); dist = dist < 0 ? 0 : (dist > 128 ? 128 : dist);
;                         const float v = __builtin_fmaf(s[r], C1, LUT[h * 132 + dist]); s[r] = v; vmax = fmaxf(vmax, v); }
;                     { float x0, x1; swap32(vmax, x0, x1); vmax = fmaxf(x0, x1); }
;                     mn = fmaxf(m, vmax);
;                     if (__all(mn - m <= AT_DEFER)) mn = m;
; #pragma unroll
;                     for (int r = 0; r < 16; ++r) { const float p = __builtin_amdgcn_exp2f(s[r] - mn);
;                         const float pmk = __builtin_bit_cast(float, __builtin_bit_cast(unsigned, p) & (unsigned)__builtin_amdgcn_sbfe((int)mwh, (r & 3) + 8 * (r >> 2), 1));
;                         s[r] = pmk; rs += pmk; }
;                 }
.LBB0_561:
	v_cmp_eq_u32_e64 s[60:61], 1, v199
	v_cmp_ne_u32_e64 s[58:59], 0, v198
	v_cmp_ne_u32_e64 s[56:57], 0, v242
	v_cmp_ne_u32_e64 s[54:55], 0, v250
	v_cmp_ne_u32_e64 s[52:53], 0, v249
	v_cmp_ne_u32_e64 s[50:51], 0, v248
	v_cmp_ne_u32_e64 s[48:49], 0, v244
	v_cmp_ne_u32_e64 s[46:47], 0, v243
	v_cmp_ne_u32_e64 s[44:45], 0, v241
	v_cmp_ne_u32_e64 s[42:43], 0, v240
	v_cmp_ne_u32_e64 s[40:41], 0, v239
	v_cmp_ne_u32_e64 s[38:39], 0, v238
	v_cmp_ne_u32_e64 s[36:37], 0, v237
	v_cmp_ne_u32_e64 s[2:3], 0, v236
	v_cmp_ne_u32_e32 vcc, 0, v235
	v_add_u32_e32 v80, s14, v231
	v_add_u32_e32 v82, -1, v80
	v_add_u32_e32 v83, -2, v80
	v_add_u32_e32 v84, -3, v80
	v_add_u32_e32 v85, -8, v80
	v_add_u32_e32 v86, -9, v80
	v_add_u32_e32 v87, -10, v80
	v_add_u32_e32 v88, -11, v80
	v_med3_i32 v81, v80, 0, v245
	v_med3_i32 v82, v82, 0, v245
	v_med3_i32 v83, v83, 0, v245
	v_med3_i32 v84, v84, 0, v245
	v_med3_i32 v85, v85, 0, v245
	v_med3_i32 v86, v86, 0, v245
	v_med3_i32 v87, v87, 0, v245
	v_med3_i32 v88, v88, 0, v245
	v_lshl_add_u32 v81, v81, 2, s9
	v_lshl_add_u32 v82, v82, 2, s9
	v_lshl_add_u32 v83, v83, 2, s9
	v_lshl_add_u32 v84, v84, 2, s9
	v_lshl_add_u32 v85, v85, 2, s9
	v_lshl_add_u32 v86, v86, 2, s9
	v_lshl_add_u32 v87, v87, 2, s9
	v_lshl_add_u32 v88, v88, 2, s9
	ds_read_b32 v81, v81
	ds_read_b32 v82, v82
	ds_read_b32 v83, v83
	ds_read_b32 v84, v84
	ds_read_b32 v85, v85
	ds_read_b32 v86, v86
	ds_read_b32 v87, v87
	ds_read_b32 v88, v88
	v_add_u32_e32 v90, -16, v80
	v_subrev_u32_e32 v91, 17, v80
	v_subrev_u32_e32 v92, 18, v80
	v_subrev_u32_e32 v93, 19, v80
	v_subrev_u32_e32 v94, 24, v80
	v_subrev_u32_e32 v95, 25, v80
	v_subrev_u32_e32 v194, 26, v80
	s_waitcnt lgkmcnt(7)
	v_fmac_f32_e32 v81, 0x3e0293ee, v64
	s_waitcnt lgkmcnt(6)
	v_fmac_f32_e32 v82, 0x3e0293ee, v65
	v_med3_i32 v90, v90, 0, v245
	v_med3_i32 v91, v91, 0, v245
	v_med3_i32 v92, v92, 0, v245
	v_med3_i32 v93, v93, 0, v245
	v_med3_i32 v94, v94, 0, v245
	v_med3_i32 v95, v95, 0, v245
	v_med3_i32 v194, v194, 0, v245
	v_subrev_u32_e32 v80, 27, v80
	v_max3_f32 v89, v81, s20, v82
	s_waitcnt lgkmcnt(5)
	v_fmac_f32_e32 v83, 0x3e0293ee, v66
	s_waitcnt lgkmcnt(4)
	v_fmac_f32_e32 v84, 0x3e0293ee, v67
	v_lshl_add_u32 v90, v90, 2, s9
	v_lshl_add_u32 v91, v91, 2, s9
	v_lshl_add_u32 v92, v92, 2, s9
	v_lshl_add_u32 v93, v93, 2, s9
	v_lshl_add_u32 v94, v94, 2, s9
	v_lshl_add_u32 v95, v95, 2, s9
	v_lshl_add_u32 v194, v194, 2, s9
	v_med3_i32 v80, v80, 0, v245
	v_max3_f32 v89, v89, v83, v84
	s_waitcnt lgkmcnt(3)
	v_fmac_f32_e32 v85, 0x3e0293ee, v68
	s_waitcnt lgkmcnt(2)
	v_fmac_f32_e32 v86, 0x3e0293ee, v69
	v_lshl_add_u32 v80, v80, 2, s9
	ds_read_b32 v90, v90
	ds_read_b32 v91, v91
	ds_read_b32 v92, v92
	ds_read_b32 v93, v93
	ds_read_b32 v94, v94
	ds_read_b32 v95, v95
	ds_read_b32 v194, v194
	ds_read_b32 v195, v80
	v_max3_f32 v89, v89, v85, v86
	s_waitcnt lgkmcnt(9)
	v_fmac_f32_e32 v87, 0x3e0293ee, v70
	s_waitcnt lgkmcnt(8)
	v_fmac_f32_e32 v88, 0x3e0293ee, v71
	v_max3_f32 v89, v89, v87, v88
	s_waitcnt lgkmcnt(7)
	v_fmac_f32_e32 v90, 0x3e0293ee, v72
	s_waitcnt lgkmcnt(6)
	v_fmac_f32_e32 v91, 0x3e0293ee, v73
	v_max3_f32 v80, v89, v90, v91
	s_waitcnt lgkmcnt(5)
	v_fmac_f32_e32 v92, 0x3e0293ee, v74
	s_waitcnt lgkmcnt(4)
	v_fmac_f32_e32 v93, 0x3e0293ee, v75
	v_max3_f32 v80, v80, v92, v93
	s_waitcnt lgkmcnt(3)
	v_fmac_f32_e32 v94, 0x3e0293ee, v76
	s_waitcnt lgkmcnt(2)
	v_fmac_f32_e32 v95, 0x3e0293ee, v77
	v_max3_f32 v80, v80, v94, v95
	s_waitcnt lgkmcnt(1)
	v_fmac_f32_e32 v194, 0x3e0293ee, v78
	s_waitcnt lgkmcnt(0)
	v_fmac_f32_e32 v195, 0x3e0293ee, v79
	v_max3_f32 v80, v80, v194, v195
	v_mov_b32_e32 v89, v80
	s_nop 1
	v_permlane32_swap_b32_e32 v80, v89
	v_max3_f32 v80, v234, v80, v89
	v_sub_f32_e32 v89, v80, v234
	v_cmp_ge_f32_e64 s[4:5], s65, v89
	s_cmp_eq_u64 s[4:5], exec
	s_cselect_b64 s[4:5], -1, 0
	v_cndmask_b32_e64 v232, v80, v234, s[4:5]
	v_sub_f32_e32 v80, v81, v232
	v_exp_f32_e32 v80, v80
	v_sub_f32_e32 v81, v82, v232
	v_exp_f32_e32 v81, v81
	v_sub_f32_e32 v82, v83, v232
	v_exp_f32_e32 v82, v82
	v_sub_f32_e32 v84, v84, v232
	v_sub_f32_e32 v85, v85, v232
	v_exp_f32_e32 v84, v84
	v_exp_f32_e32 v85, v85
	v_cndmask_b32_e64 v80, 0, v80, s[60:61]
	v_add_f32_e32 v83, 0, v80
	v_cndmask_b32_e64 v81, 0, v81, s[58:59]
	v_add_f32_e32 v83, v81, v83
	v_cndmask_b32_e64 v82, 0, v82, s[56:57]
	v_add_f32_e32 v89, v82, v83
	v_cndmask_b32_e64 v83, 0, v84, s[54:55]
	v_cndmask_b32_e64 v84, 0, v85, s[52:53]
	v_sub_f32_e32 v85, v86, v232
	v_add_f32_e32 v89, v83, v89
	v_exp_f32_e32 v85, v85
	v_sub_f32_e32 v86, v87, v232
	v_exp_f32_e32 v86, v86
	v_add_f32_e32 v87, v84, v89
	v_sub_f32_e32 v88, v88, v232
	v_sub_f32_e32 v89, v90, v232
	v_exp_f32_e32 v88, v88
	v_exp_f32_e32 v89, v89
	v_cndmask_b32_e64 v85, 0, v85, s[50:51]
	v_add_f32_e32 v87, v85, v87
	v_cndmask_b32_e64 v86, 0, v86, s[48:49]
	v_add_f32_e32 v90, v86, v87
	v_cndmask_b32_e64 v87, 0, v88, s[46:47]
	v_cndmask_b32_e64 v88, 0, v89, s[44:45]
	v_sub_f32_e32 v89, v91, v232
	v_exp_f32_e32 v89, v89
	v_sub_f32_e32 v91, v92, v232
	v_exp_f32_e32 v91, v91
	v_add_f32_e32 v90, v87, v90
	v_add_f32_e32 v90, v88, v90
	v_cndmask_b32_e64 v89, 0, v89, s[42:43]
	v_add_f32_e32 v92, v89, v90
	v_cndmask_b32_e64 v90, 0, v91, s[40:41]
	v_sub_f32_e32 v91, v93, v232
	v_exp_f32_e32 v91, v91
	v_sub_f32_e32 v93, v94, v232
	v_exp_f32_e32 v93, v93
	v_add_f32_e32 v92, v90, v92
	v_cndmask_b32_e64 v91, 0, v91, s[38:39]
	v_add_f32_e32 v94, v91, v92
	v_cndmask_b32_e64 v92, 0, v93, s[36:37]
	v_sub_f32_e32 v93, v95, v232
	v_exp_f32_e32 v93, v93
	v_sub_f32_e32 v95, v194, v232
	v_exp_f32_e32 v95, v95
	v_add_f32_e32 v94, v92, v94
	v_cndmask_b32_e64 v93, 0, v93, s[2:3]
	v_add_f32_e32 v194, v93, v94
	v_cndmask_b32_e32 v94, 0, v95, vcc
	v_add_f32_e32 v247, v94, v194
	v_sub_f32_e32 v95, v195, v232
	s_cbranch_execnz .LBB0_552
; __device__ __forceinline__ void attn_phase_mfma(Frame& F) {
;     ...
;                 if (far) {
;                     float smax = fmaxf(fmaxf(s[0], s[1]), fmaxf(s[2], s[3]));
; #pragma unroll
;                     for (int r = 4; r < 16; r += 2) smax = fmaxf(smax, fmaxf(s[r], s[r + 1]));
;                     { float x0, x1; swap32(smax, x0, x1); smax = fmaxf(x0, x1); }
;                     mn = fmaxf(m, __builtin_fmaf(smax, C1, bfar));
;                     if (__all(mn - m <= AT_DEFER)) mn = m;
;                     const float bm = bfar - mn;
; #pragma unroll
;                     for (int r = 0; r < 16; ++r) { const float p = __builtin_amdgcn_exp2f(__builtin_fmaf(s[r], C1, bm));
;                         const float pmk = __builtin_bit_cast(float, __builtin_bit_cast(unsigned, p) & (unsigned)__builtin_amdgcn_sbfe((int)mwh, (r & 3) + 8 * (r >> 2), 1));
;                         s[r] = pmk; rs += pmk; }
.LBB0_562:
	v_max3_f32 v80, v64, v65, v66
	v_max3_f32 v81, v67, v68, v69
	v_max3_f32 v80, v80, v70, v71
	v_max3_f32 v81, v81, v72, v73
	v_max3_f32 v80, v80, v74, v75
	v_max3_f32 v81, v81, v76, v77
	v_max3_f32 v80, v80, v78, v79
	v_max_f32_e32 v80, v80, v81
	v_mov_b32_e32 v81, v80
	s_nop 1
	v_permlane32_swap_b32_e32 v80, v81
	v_max_f32_e32 v81, v81, v81
	v_max_f32_e32 v80, v80, v80
	v_max_f32_e32 v80, v80, v81
	v_fmamk_f32 v80, v80, 0x3e0293ee, v211
	v_max_f32_e32 v81, v234, v234
	v_max_f32_e32 v80, v81, v80
	v_sub_f32_e32 v81, v80, v234
	v_cmp_ge_f32_e32 vcc, s65, v81
	s_cmp_eq_u64 vcc, exec
	s_cselect_b64 vcc, -1, 0
	v_cndmask_b32_e32 v232, v80, v234, vcc
	v_sub_f32_e32 v95, v211, v232
	v_fmamk_f32 v64, v64, 0x3e0293ee, v95
	v_exp_f32_e32 v64, v64
	v_fmamk_f32 v65, v65, 0x3e0293ee, v95
	v_exp_f32_e32 v65, v65
	v_fmamk_f32 v66, v66, 0x3e0293ee, v95
	v_exp_f32_e32 v66, v66
	v_cmp_eq_u32_e32 vcc, 1, v199
	s_nop 1
	v_cndmask_b32_e32 v80, 0, v64, vcc
	v_cmp_ne_u32_e32 vcc, 0, v198
	v_add_f32_e32 v64, 0, v80
	s_nop 0
	v_cndmask_b32_e32 v81, 0, v65, vcc
	v_cmp_ne_u32_e32 vcc, 0, v242
	v_fmamk_f32 v65, v67, 0x3e0293ee, v95
	v_exp_f32_e32 v65, v65
	v_cndmask_b32_e32 v82, 0, v66, vcc
	v_fmamk_f32 v66, v68, 0x3e0293ee, v95
	v_exp_f32_e32 v66, v66
	v_cmp_ne_u32_e32 vcc, 0, v250
	v_add_f32_e32 v64, v81, v64
	v_add_f32_e32 v64, v82, v64
	v_cndmask_b32_e32 v83, 0, v65, vcc
	v_cmp_ne_u32_e32 vcc, 0, v249
	v_fmamk_f32 v65, v69, 0x3e0293ee, v95
	v_exp_f32_e32 v65, v65
	v_cndmask_b32_e32 v84, 0, v66, vcc
	v_fmamk_f32 v66, v70, 0x3e0293ee, v95
	v_exp_f32_e32 v66, v66
	v_cmp_ne_u32_e32 vcc, 0, v248
	v_add_f32_e32 v64, v83, v64
	v_add_f32_e32 v64, v84, v64
	v_cndmask_b32_e32 v85, 0, v65, vcc
	v_cmp_ne_u32_e32 vcc, 0, v244
	v_fmamk_f32 v65, v71, 0x3e0293ee, v95
	v_exp_f32_e32 v65, v65
	v_cndmask_b32_e32 v86, 0, v66, vcc
	v_fmamk_f32 v66, v72, 0x3e0293ee, v95
	v_exp_f32_e32 v66, v66
	v_cmp_ne_u32_e32 vcc, 0, v243
	v_add_f32_e32 v64, v85, v64
	v_add_f32_e32 v64, v86, v64
	v_cndmask_b32_e32 v87, 0, v65, vcc
	v_cmp_ne_u32_e32 vcc, 0, v241
	v_fmamk_f32 v65, v73, 0x3e0293ee, v95
	v_exp_f32_e32 v65, v65
	v_cndmask_b32_e32 v88, 0, v66, vcc
	v_fmamk_f32 v66, v74, 0x3e0293ee, v95
	v_exp_f32_e32 v66, v66
	v_cmp_ne_u32_e32 vcc, 0, v240
	v_add_f32_e32 v64, v87, v64
	v_add_f32_e32 v64, v88, v64
	v_cndmask_b32_e32 v89, 0, v65, vcc
	v_cmp_ne_u32_e32 vcc, 0, v239
	v_fmamk_f32 v65, v75, 0x3e0293ee, v95
	v_exp_f32_e32 v65, v65
	v_cndmask_b32_e32 v90, 0, v66, vcc
	v_fmamk_f32 v66, v76, 0x3e0293ee, v95
	v_exp_f32_e32 v66, v66
	v_cmp_ne_u32_e32 vcc, 0, v238
	v_add_f32_e32 v64, v89, v64
	v_add_f32_e32 v64, v90, v64
	v_cndmask_b32_e32 v91, 0, v65, vcc
	v_cmp_ne_u32_e32 vcc, 0, v237
	v_fmamk_f32 v65, v77, 0x3e0293ee, v95
	v_exp_f32_e32 v65, v65
	v_cndmask_b32_e32 v92, 0, v66, vcc
	v_fmamk_f32 v66, v78, 0x3e0293ee, v95
	v_exp_f32_e32 v66, v66
	v_add_f32_e32 v64, v91, v64
	v_cmp_ne_u32_e32 vcc, 0, v236
	v_add_f32_e32 v64, v92, v64
	v_fmac_f32_e32 v95, 0x3e0293ee, v79
	v_cndmask_b32_e32 v93, 0, v65, vcc
	v_cmp_ne_u32_e32 vcc, 0, v235
	v_add_f32_e32 v64, v93, v64
	s_nop 0
	v_cndmask_b32_e32 v94, 0, v66, vcc
	v_add_f32_e32 v247, v94, v64
	v_cmp_neq_f32_e32 vcc, v232, v234
	s_mov_b64 s[52:53], 0x2000
	s_cbranch_vccnz .LBB0_553
	s_branch .LBB0_554
